# kpe projection loop: all 24 operand loads of an iteration issued up front, counted vmcnt before each MFMA pair
# speedup vs baseline: 1.0031x; 1.0031x over previous
.LBB0_262:
	v_lshl_add_u64 v[66:67], v[44:45], 0, s[0:1]
	v_lshl_add_u64 v[68:69], v[36:37], 0, s[0:1]
	v_add_co_u32_e32 v70, vcc, s5, v68
	s_nop 1
	v_addc_co_u32_e32 v71, vcc, 0, v69, vcc
	global_load_dwordx4 v[72:75], v[66:67], off
	global_load_dwordx4 v[76:79], v[68:69], off
	global_load_dwordx4 v[80:83], v[70:71], off
	global_load_dwordx4 v[84:87], v[66:67], off offset:32
	global_load_dwordx4 v[88:91], v[68:69], off offset:32
	global_load_dwordx4 v[92:95], v[70:71], off offset:32
	global_load_dwordx4 v[96:99], v[66:67], off offset:64
	global_load_dwordx4 v[100:103], v[68:69], off offset:64
	global_load_dwordx4 v[104:107], v[70:71], off offset:64
	global_load_dwordx4 v[108:111], v[66:67], off offset:96
	global_load_dwordx4 v[112:115], v[68:69], off offset:96
	global_load_dwordx4 v[116:119], v[70:71], off offset:96
	global_load_dwordx4 v[120:123], v[66:67], off offset:128
	global_load_dwordx4 v[156:159], v[68:69], off offset:128
	global_load_dwordx4 v[160:163], v[70:71], off offset:128
	global_load_dwordx4 v[164:167], v[66:67], off offset:160
	global_load_dwordx4 v[168:171], v[68:69], off offset:160
	global_load_dwordx4 v[172:175], v[70:71], off offset:160
	global_load_dwordx4 v[176:179], v[66:67], off offset:192
	global_load_dwordx4 v[180:183], v[68:69], off offset:192
	global_load_dwordx4 v[184:187], v[70:71], off offset:192
	global_load_dwordx4 v[188:191], v[66:67], off offset:224
	global_load_dwordx4 v[192:195], v[68:69], off offset:224
	global_load_dwordx4 v[196:199], v[70:71], off offset:224
	s_add_u32 s0, s0, 0x100
	s_addc_u32 s1, s1, 0
	s_cmpk_eq_i32 s0, 0x200
	s_waitcnt vmcnt(21)
	v_mfma_f32_32x32x16_bf16 v[2:17], v[72:75], v[76:79], v[2:17]
	v_mfma_f32_32x32x16_bf16 v[18:33], v[72:75], v[80:83], v[18:33]
	s_waitcnt vmcnt(18)
	v_mfma_f32_32x32x16_bf16 v[2:17], v[84:87], v[88:91], v[2:17]
	v_mfma_f32_32x32x16_bf16 v[18:33], v[84:87], v[92:95], v[18:33]
	s_waitcnt vmcnt(15)
	v_mfma_f32_32x32x16_bf16 v[2:17], v[96:99], v[100:103], v[2:17]
	v_mfma_f32_32x32x16_bf16 v[18:33], v[96:99], v[104:107], v[18:33]
	s_waitcnt vmcnt(12)
	v_mfma_f32_32x32x16_bf16 v[2:17], v[108:111], v[112:115], v[2:17]
	v_mfma_f32_32x32x16_bf16 v[18:33], v[108:111], v[116:119], v[18:33]
	s_waitcnt vmcnt(9)
	v_mfma_f32_32x32x16_bf16 v[2:17], v[120:123], v[156:159], v[2:17]
	v_mfma_f32_32x32x16_bf16 v[18:33], v[120:123], v[160:163], v[18:33]
	s_waitcnt vmcnt(6)
	v_mfma_f32_32x32x16_bf16 v[2:17], v[164:167], v[168:171], v[2:17]
	v_mfma_f32_32x32x16_bf16 v[18:33], v[164:167], v[172:175], v[18:33]
	s_waitcnt vmcnt(3)
	v_mfma_f32_32x32x16_bf16 v[2:17], v[176:179], v[180:183], v[2:17]
	v_mfma_f32_32x32x16_bf16 v[18:33], v[176:179], v[184:187], v[18:33]
	s_waitcnt vmcnt(0)
	v_mfma_f32_32x32x16_bf16 v[2:17], v[188:191], v[192:195], v[2:17]
	v_mfma_f32_32x32x16_bf16 v[18:33], v[188:191], v[196:199], v[18:33]
	s_cbranch_scc0 .LBB0_262
	v_add_u32_e32 v43, s2, v1
	s_nop 6
	ds_write2st64_b32 v43, v2, v3 offset1:1
	s_nop 1
	ds_write2st64_b32 v43, v18, v19 offset0:16 offset1:17
	ds_write2st64_b32 v43, v4, v5 offset0:2 offset1:3
	ds_write2st64_b32 v43, v20, v21 offset0:18 offset1:19
	ds_write2st64_b32 v43, v6, v7 offset0:4 offset1:5
	ds_write2st64_b32 v43, v22, v23 offset0:20 offset1:21
	ds_write2st64_b32 v43, v8, v9 offset0:6 offset1:7
	ds_write2st64_b32 v43, v24, v25 offset0:22 offset1:23
	ds_write2st64_b32 v43, v10, v11 offset0:8 offset1:9
	ds_write2st64_b32 v43, v26, v27 offset0:24 offset1:25
	ds_write2st64_b32 v43, v12, v13 offset0:10 offset1:11
	ds_write2st64_b32 v43, v28, v29 offset0:26 offset1:27
	ds_write2st64_b32 v43, v14, v15 offset0:12 offset1:13
	ds_write2st64_b32 v43, v30, v31 offset0:28 offset1:29
	ds_write2st64_b32 v43, v16, v17 offset0:14 offset1:15
	ds_write2st64_b32 v43, v32, v33 offset0:30 offset1:31
	v_lshl_or_b32 v20, s62, 5, v48
	v_or_b32_e32 v2, v20, v47
	v_ashrrev_i32_e32 v3, 31, v2
	v_lshlrev_b64 v[2:3], 7, v[2:3]
	v_or_b32_e32 v4, v2, v34
	v_mov_b32_e32 v5, v3
	v_lshl_add_u64 v[6:7], s[14:15], 0, v[4:5]
	s_waitcnt lgkmcnt(0)
	s_barrier
	global_load_dword v21, v[6:7], off
	v_lshl_add_u64 v[4:5], s[12:13], 0, v[4:5]
	global_load_dword v22, v[4:5], off
	ds_read2st64_b32 v[4:5], v46 offset1:32
	ds_read2st64_b32 v[6:7], v51 offset0:16 offset1:48
	ds_read2st64_b32 v[8:9], v46 offset0:64 offset1:96
	ds_read2st64_b32 v[10:11], v51 offset0:80 offset1:112
	ds_read2st64_b32 v[12:13], v46 offset0:128 offset1:160
	ds_read2st64_b32 v[14:15], v51 offset0:144 offset1:176
	ds_read2st64_b32 v[16:17], v46 offset0:192 offset1:224
	ds_read2st64_b32 v[18:19], v51 offset0:208 offset1:240
	s_waitcnt lgkmcnt(7)
	v_add_f32_e32 v4, 0, v4
	s_waitcnt lgkmcnt(6)
	v_add_f32_e32 v6, 0, v6
	v_add_f32_e32 v4, v4, v5
	v_add_f32_e32 v5, v6, v7
	s_waitcnt lgkmcnt(5)
	v_add_f32_e32 v4, v4, v8
	s_waitcnt lgkmcnt(4)
	v_add_f32_e32 v5, v5, v10
	v_add_f32_e32 v4, v4, v9
	v_add_f32_e32 v5, v5, v11
	s_waitcnt lgkmcnt(3)
	v_add_f32_e32 v4, v4, v12
	s_waitcnt lgkmcnt(2)
	v_add_f32_e32 v5, v5, v14
	v_add_f32_e32 v4, v4, v13
	v_add_f32_e32 v5, v5, v15
	s_waitcnt lgkmcnt(1)
	v_add_f32_e32 v4, v4, v16
	s_waitcnt lgkmcnt(0)
	v_add_f32_e32 v5, v5, v18
	v_add_f32_e32 v4, v4, v17
	v_add_f32_e32 v5, v5, v19
	v_mov_b32_e32 v23, 0
	v_add_u32_e32 v20, v20, v50
	v_lshl_add_u64 v[2:3], v[38:39], 0, v[2:3]
	s_add_i32 s62, s62, s82
	s_cmpk_gt_i32 s62, 0x1ff
	v_add_u32_e32 v42, s3, v42
	s_waitcnt vmcnt(1)
	v_mul_f32_e32 v6, v5, v21
	v_mul_f32_e32 v7, v4, v21
	s_waitcnt vmcnt(0)
	v_fma_f32 v4, v4, v22, -v6
	v_fmac_f32_e32 v7, v5, v22
	v_mul_f32_e32 v4, 0x41000000, v4
	v_mul_f32_e32 v5, 0x41000000, v7
	v_med3_f32 v4, v4, s4, v53
	v_med3_f32 v5, v5, s4, v53
	v_cvt_pk_fp8_f32 v23, v4, v5
	v_ashrrev_i32_e32 v21, 31, v20
	v_lshlrev_b64 v[4:5], 7, v[20:21]
	v_or_b32_e32 v6, v4, v34
	v_cvt_pk_fp8_f32 v23, 0, 0 op_sel:[0,0,1]
	v_mov_b32_e32 v7, v5
	v_lshl_add_u64 v[8:9], s[14:15], 0, v[6:7]
	v_mov_b32_e32 v22, 0
	v_lshrrev_b32_e32 v10, 8, v23
	global_store_byte v[2:3], v23, off
	global_store_byte v[2:3], v10, off offset:32
	global_load_dword v20, v[8:9], off
	v_lshl_add_u64 v[2:3], s[12:13], 0, v[6:7]
	global_load_dword v21, v[2:3], off
	ds_read2st64_b32 v[2:3], v49 offset1:32
	ds_read2st64_b32 v[6:7], v52 offset0:16 offset1:48
	ds_read2st64_b32 v[8:9], v49 offset0:64 offset1:96
	ds_read2st64_b32 v[10:11], v52 offset0:80 offset1:112
	ds_read2st64_b32 v[12:13], v49 offset0:128 offset1:160
	ds_read2st64_b32 v[14:15], v52 offset0:144 offset1:176
	ds_read2st64_b32 v[16:17], v49 offset0:192 offset1:224
	ds_read2st64_b32 v[18:19], v52 offset0:208 offset1:240
	s_waitcnt lgkmcnt(7)
	v_add_f32_e32 v2, 0, v2
	s_waitcnt lgkmcnt(6)
	v_add_f32_e32 v6, 0, v6
	v_add_f32_e32 v2, v2, v3
	v_add_f32_e32 v3, v6, v7
	s_waitcnt lgkmcnt(5)
	v_add_f32_e32 v2, v2, v8
	s_waitcnt lgkmcnt(4)
	v_add_f32_e32 v3, v3, v10
	v_add_f32_e32 v2, v2, v9
	v_add_f32_e32 v3, v3, v11
	s_waitcnt lgkmcnt(3)
	v_add_f32_e32 v2, v2, v12
	s_waitcnt lgkmcnt(2)
	v_add_f32_e32 v3, v3, v14
	v_add_f32_e32 v2, v2, v13
	v_add_f32_e32 v3, v3, v15
	s_waitcnt lgkmcnt(1)
	v_add_f32_e32 v2, v2, v16
	s_waitcnt lgkmcnt(0)
	v_add_f32_e32 v3, v3, v18
	v_add_f32_e32 v2, v2, v17
	v_add_f32_e32 v3, v3, v19
	s_waitcnt vmcnt(1)
	v_mul_f32_e32 v6, v3, v20
	v_mul_f32_e32 v7, v2, v20
	s_waitcnt vmcnt(0)
	v_fma_f32 v2, v2, v21, -v6
	v_fmac_f32_e32 v7, v3, v21
	v_mul_f32_e32 v2, 0x41000000, v2
	v_mul_f32_e32 v3, 0x41000000, v7
	v_med3_f32 v2, v2, s4, v53
	v_med3_f32 v3, v3, s4, v53
	v_cvt_pk_fp8_f32 v22, v2, v3
	v_lshl_add_u64 v[2:3], v[38:39], 0, v[4:5]
	v_cvt_pk_fp8_f32 v22, 0, 0 op_sel:[0,0,1]
	s_nop 0
	v_lshrrev_b32_e32 v4, 8, v22
	global_store_byte v[2:3], v22, off
	global_store_byte v[2:3], v4, off offset:32
	s_barrier
	s_cbranch_scc0 .LBB0_261
